# attention phase balance: WGs 0-15 (two scan-C items) claim 5 fewer background conversion steps; on top of cvt_pk + gates epilogue
# speedup vs baseline: 1.0090x; 1.0090x over previous
; #define LAS __attribute__((address_space(3)))
; #define PHASE_BEGIN() Ctx c = c0; { int t_ = c0.tid; asm volatile("" : "+v"(t_)); c.tid = t_; c.lane = t_ & 63; c.wave = __builtin_amdgcn_readfirstlane(t_ >> 6); } \
;     GAS unsigned char* wsb = (GAS unsigned char*)a.ws; asm volatile("" : "+s"(wsb));
; __device__ __forceinline__ void bg_take(const Args& a, const Ctx& c0, int n) {
;     PHASE_BEGIN();
;     unsigned* head = WSP(unsigned, WS_CTL) + CW_QHEAD;
;     volatile LAS unsigned* bc = (volatile LAS unsigned*)(c.lds + LDS_MISC + 64);
;     LAS float* scr = (LAS float*)(c.lds + c.wave * 16640);
;     __syncthreads();
;     for (int i = 0; i < n; ++i) {
;         if (c.tid == 0) { unsigned s = __hip_atomic_fetch_add(head, 1u, __ATOMIC_RELAXED, __HIP_MEMORY_SCOPE_AGENT); if (s >= (unsigned)BG_STEPS) s = 0xffffffffu; bc[0] = s; }
; __global__ void __launch_bounds__(512, 2) mk_fwd(Args a) {
;     ...
;         if (IN(pb + 5) && (c.bid & 1) == 0) { if (l == 0) mod_items(a, c, 1); bg_take(a, c, l == 0 ? 26 : 24); }
;         if (EN(5) && IN(pb + 5)) for (int rep = 0; rep < NREP(5); ++rep) { phase_attn(a, c, l, last); }
;         if (IN(pb + 5) && (c.bid & 1) == 1) { bg_take(a, c, l == 0 ? 26 : 24); if (l == 0) mod_items(a, c, 1); }
.LBB0_1254:
	s_cmp_lt_u32 s90, 16
	s_cbranch_scc0 .Lbal1
	s_add_i32 s14, s14, -5

; #define LAS __attribute__((address_space(3)))
; #define PHASE_BEGIN() Ctx c = c0; { int t_ = c0.tid; asm volatile("" : "+v"(t_)); c.tid = t_; c.lane = t_ & 63; c.wave = __builtin_amdgcn_readfirstlane(t_ >> 6); } \
;     GAS unsigned char* wsb = (GAS unsigned char*)a.ws; asm volatile("" : "+s"(wsb));
; __device__ __forceinline__ void bg_take(const Args& a, const Ctx& c0, int n) {
;     PHASE_BEGIN();
;     unsigned* head = WSP(unsigned, WS_CTL) + CW_QHEAD;
;     volatile LAS unsigned* bc = (volatile LAS unsigned*)(c.lds + LDS_MISC + 64);
;     LAS float* scr = (LAS float*)(c.lds + c.wave * 16640);
;     __syncthreads();
; __global__ void __launch_bounds__(512, 2) mk_fwd(Args a) {
;     ...
;         if (IN(pb + 5) && (c.bid & 1) == 0) { if (l == 0) mod_items(a, c, 1); bg_take(a, c, l == 0 ? 26 : 24); }
;         if (EN(5) && IN(pb + 5)) for (int rep = 0; rep < NREP(5); ++rep) { phase_attn(a, c, l, last); }
;         if (IN(pb + 5) && (c.bid & 1) == 1) { bg_take(a, c, l == 0 ? 26 : 24); if (l == 0) mod_items(a, c, 1); }
.LBB0_1493:
	v_readlane_b32 s2, v252, 54
	v_readlane_b32 s3, v252, 55
	s_andn2_b64 vcc, exec, s[2:3]
	s_cbranch_vccnz .LBB0_1700
	v_readlane_b32 s2, v254, 54
	v_readlane_b32 s3, v254, 55
	s_and_b64 s[2:3], s[2:3], exec
	v_mov_b32_e32 v1, v0
	v_readlane_b32 s4, v254, 21
	v_readlane_b32 s5, v254, 22
	v_readfirstlane_b32 s2, v1
	v_readlane_b32 s6, v254, 23
	v_readlane_b32 s7, v254, 24
	s_cselect_b32 s10, 26, 24
	s_cmp_lt_u32 s90, 16
	s_cbranch_scc0 .Lbal2
	s_add_i32 s10, s10, -5
.Lbal2:
	s_ashr_i32 s11, s2, 6
	s_mov_b64 s[4:5], s[6:7]
	v_lshlrev_b32_e32 v2, 2, v1
	s_add_u32 s2, s4, 0x8000
	s_mul_i32 s6, s11, 0x4100
	v_bfe_u32 v67, v1, 4, 2
	v_and_b32_e32 v66, 60, v2
	s_addc_u32 s3, s5, 0
	s_add_i32 s6, s6, 0
	v_cmp_eq_u32_e64 s[38:39], 0, v1
	v_mul_u32_u24_e32 v2, 0x104, v67
	s_waitcnt lgkmcnt(0)
	v_lshlrev_b32_e32 v3, 2, v66
	v_bfe_u32 v96, v1, 3, 3
	v_lshlrev_b32_e32 v1, 3, v1
	v_add3_u32 v95, s6, v2, v3
	v_and_b32_e32 v2, 56, v1
	v_mov_b32_e32 v3, v147
	v_mul_u32_u24_e32 v1, 0x104, v2
	v_lshl_add_u64 v[4:5], s[4:5], 0, v[2:3]
	v_lshlrev_b32_e32 v3, 2, v96
	v_add3_u32 v97, s6, v1, v3
	v_lshlrev_b32_e32 v2, 1, v2
	v_mov_b32_e32 v3, v147
	v_lshl_add_u64 v[2:3], s[4:5], 0, v[2:3]
	s_mov_b64 s[4:5], 0x1bc00000
	v_lshl_add_u64 v[72:73], v[2:3], 0, s[4:5]
	s_mov_b64 s[4:5], 0x1b800000
	v_lshl_add_u64 v[74:75], v[2:3], 0, s[4:5]
	s_mov_b64 s[4:5], 0x1b600000
	v_lshl_add_u64 v[76:77], v[2:3], 0, s[4:5]
	s_mov_b64 s[4:5], 0x1aa00000
	v_lshl_add_u64 v[78:79], v[2:3], 0, s[4:5]
	s_mov_b64 s[4:5], 0x12a00000
	v_lshl_add_u64 v[80:81], v[4:5], 0, s[4:5]
	s_mov_b64 s[4:5], 0x2a00000
	v_lshl_add_u64 v[82:83], v[4:5], 0, s[4:5]
	s_mov_b64 s[4:5], 0x2200000
	v_lshl_add_u64 v[84:85], v[2:3], 0, s[4:5]
	s_mov_b64 s[4:5], 0x1e00000
	v_lshl_add_u64 v[86:87], v[2:3], 0, s[4:5]
	s_mov_b64 s[4:5], 0x1c00000
	s_mov_b64 s[8:9], 0x2c400000
	s_mov_b64 s[6:7], 0x1c400000
	v_lshl_add_u64 v[88:89], v[2:3], 0, s[4:5]
	s_mov_b64 s[4:5], 0x1000000
	v_lshl_add_u64 v[68:69], v[4:5], 0, s[8:9]
	v_or_b32_e32 v98, 8, v96
	v_or_b32_e32 v99, 16, v96
	v_or_b32_e32 v100, 24, v96
	v_or_b32_e32 v101, 32, v96
	v_or_b32_e32 v102, 40, v96
	v_or_b32_e32 v103, 48, v96
	v_or_b32_e32 v104, 56, v96
	v_lshl_add_u64 v[70:71], v[4:5], 0, s[6:7]
	v_lshl_add_u64 v[90:91], v[2:3], 0, s[4:5]
	s_waitcnt vmcnt(0)
	s_barrier
	s_branch .LBB0_1496
